# speedup vs baseline: 1.0727x; 1.0147x over previous
.Lg_top:
	s_cmp_gt_u32 s10, s9
	s_cbranch_scc1 .Lg_noprep0
	v_readlane_b32 s13, v247, s10
	s_add_u32 s14, s12, 0x4b0
	s_add_u32 s15, s12, 0x960
	s_add_u32 s16, s12, 0xe10
	s_nop 1
	s_and_b32 s18, s13, 0xff
	s_cmp_eq_u32 s18, 1
	s_cselect_b32 s42, s12, 0x80000000
	s_and_b32 s18, s13, 0xff00
	s_cmp_eq_u32 s18, 0x100
	s_cselect_b32 s14, s14, 0x80000000
	s_and_b32 s18, s13, 0xff0000
	s_cmp_eq_u32 s18, 0x10000
	s_cselect_b32 s15, s15, 0x80000000
	s_and_b32 s18, s13, 0xff000000
	s_cmp_eq_u32 s18, 0x1000000
	s_cselect_b32 s16, s16, 0x80000000
	v_lshrrev_b32_e64 v249, v240, s13
	v_and_b32_e32 v249, 0xff, v249
	v_cmp_eq_u32_e32 vcc, 1, v249
	s_nop 1
	v_cndmask_b32_e32 v254, v255, v239, vcc
.Lg_noprep0:
	s_sub_u32 s18, s10, 2
	s_cmp_lt_u32 s18, s9
	s_cbranch_scc0 .Lg_s2skip0
	s_cmp_gt_u32 s10, s9
	s_cbranch_scc1 .Lg_s2final0
	s_waitcnt vmcnt(21)
	v_cvt_pk_f16_f32 v250, v138, v139
	v_cvt_pk_f16_f32 v251, v140, v141
	ds_write_b64 v241, v[250:251] offset:0
	buffer_load_dwordx4 v[138:141], v238, s[20:23], s42 offen nt
	s_waitcnt vmcnt(21)
	v_cvt_pk_f16_f32 v252, v142, v143
	v_cvt_pk_f16_f32 v253, v144, v145
	ds_write_b64 v241, v[252:253] offset:600
	buffer_load_dwordx4 v[142:145], v238, s[24:27], s42 offen nt
	s_waitcnt vmcnt(21)
	v_cvt_pk_f16_f32 v250, v146, v147
	v_cvt_pk_f16_f32 v251, v148, v149
	ds_write_b64 v241, v[250:251] offset:1248
	buffer_load_dwordx4 v[146:149], v238, s[20:23], s14 offen nt
	s_waitcnt vmcnt(21)
	v_cvt_pk_f16_f32 v252, v150, v151
	v_cvt_pk_f16_f32 v253, v152, v153
	ds_write_b64 v241, v[252:253] offset:1848
	buffer_load_dwordx4 v[150:153], v238, s[24:27], s14 offen nt
	s_waitcnt vmcnt(21)
	v_cvt_pk_f16_f32 v250, v154, v155
	v_cvt_pk_f16_f32 v251, v156, v157
	ds_write_b64 v241, v[250:251] offset:2496
	buffer_load_dwordx4 v[154:157], v238, s[20:23], s15 offen nt
	s_waitcnt vmcnt(21)
	v_cvt_pk_f16_f32 v252, v158, v159
	v_cvt_pk_f16_f32 v253, v160, v161
	ds_write_b64 v241, v[252:253] offset:3096
	buffer_load_dwordx4 v[158:161], v238, s[24:27], s15 offen nt
	s_waitcnt vmcnt(21)
	v_cvt_pk_f16_f32 v250, v162, v163
	v_cvt_pk_f16_f32 v251, v164, v165
	ds_write_b64 v241, v[250:251] offset:3744
	buffer_load_dwordx4 v[162:165], v238, s[20:23], s16 offen nt
	s_waitcnt vmcnt(21)
	v_cvt_pk_f16_f32 v252, v166, v167
	v_cvt_pk_f16_f32 v253, v168, v169
	ds_write_b64 v241, v[252:253] offset:4344
	buffer_load_dwordx4 v[166:169], v238, s[24:27], s16 offen nt
	s_mov_b64 exec, s[34:35]
	s_waitcnt vmcnt(21)
	v_cvt_pk_f16_f32 v250, v170, v171
	v_cvt_pk_f16_f32 v251, v172, v173
	ds_write_b64 v242, v[250:251] offset:0
	s_mov_b64 exec, -1
	buffer_load_dwordx4 v[170:173], v254, s[20:23], s12 offen nt
	s_mov_b64 exec, s[34:35]
	s_waitcnt vmcnt(21)
	v_cvt_pk_f16_f32 v252, v174, v175
	v_cvt_pk_f16_f32 v253, v176, v177
	ds_write_b64 v242, v[252:253] offset:600
	s_mov_b64 exec, -1
	buffer_load_dwordx4 v[174:177], v254, s[24:27], s12 offen nt
	s_branch .Lg_s1done0
.Lg_s2final0:
	s_waitcnt vmcnt(21)
	v_cvt_pk_f16_f32 v250, v138, v139
	v_cvt_pk_f16_f32 v251, v140, v141
	ds_write_b64 v241, v[250:251] offset:0
	s_waitcnt vmcnt(20)
	v_cvt_pk_f16_f32 v252, v142, v143
	v_cvt_pk_f16_f32 v253, v144, v145
	ds_write_b64 v241, v[252:253] offset:600
	s_waitcnt vmcnt(19)
	v_cvt_pk_f16_f32 v250, v146, v147
	v_cvt_pk_f16_f32 v251, v148, v149
	ds_write_b64 v241, v[250:251] offset:1248
	s_waitcnt vmcnt(18)
	v_cvt_pk_f16_f32 v252, v150, v151
	v_cvt_pk_f16_f32 v253, v152, v153
	ds_write_b64 v241, v[252:253] offset:1848
	s_waitcnt vmcnt(17)
	v_cvt_pk_f16_f32 v250, v154, v155
	v_cvt_pk_f16_f32 v251, v156, v157
	ds_write_b64 v241, v[250:251] offset:2496
	s_waitcnt vmcnt(16)
	v_cvt_pk_f16_f32 v252, v158, v159
	v_cvt_pk_f16_f32 v253, v160, v161
	ds_write_b64 v241, v[252:253] offset:3096
	s_waitcnt vmcnt(15)
	v_cvt_pk_f16_f32 v250, v162, v163
	v_cvt_pk_f16_f32 v251, v164, v165
	ds_write_b64 v241, v[250:251] offset:3744
	s_waitcnt vmcnt(14)
	v_cvt_pk_f16_f32 v252, v166, v167
	v_cvt_pk_f16_f32 v253, v168, v169
	ds_write_b64 v241, v[252:253] offset:4344
	s_mov_b64 exec, s[34:35]
	s_waitcnt vmcnt(13)
	v_cvt_pk_f16_f32 v250, v170, v171
	v_cvt_pk_f16_f32 v251, v172, v173
	ds_write_b64 v242, v[250:251] offset:0
	s_mov_b64 exec, -1
	s_mov_b64 exec, s[34:35]
	s_waitcnt vmcnt(12)
	v_cvt_pk_f16_f32 v252, v174, v175
	v_cvt_pk_f16_f32 v253, v176, v177
	ds_write_b64 v242, v[252:253] offset:600
	s_mov_b64 exec, -1
	s_branch .Lg_s1done0
.Lg_s2skip0:
	s_cmp_gt_u32 s10, s9
	s_cbranch_scc1 .Lg_s1done0
	buffer_load_dwordx4 v[138:141], v238, s[20:23], s42 offen nt
	buffer_load_dwordx4 v[142:145], v238, s[24:27], s42 offen nt
	buffer_load_dwordx4 v[146:149], v238, s[20:23], s14 offen nt
	buffer_load_dwordx4 v[150:153], v238, s[24:27], s14 offen nt
	buffer_load_dwordx4 v[154:157], v238, s[20:23], s15 offen nt
	buffer_load_dwordx4 v[158:161], v238, s[24:27], s15 offen nt
	buffer_load_dwordx4 v[162:165], v238, s[20:23], s16 offen nt
	buffer_load_dwordx4 v[166:169], v238, s[24:27], s16 offen nt
	buffer_load_dwordx4 v[170:173], v254, s[20:23], s12 offen nt
	buffer_load_dwordx4 v[174:177], v254, s[24:27], s12 offen nt

.Lg_noprep1:
	s_sub_u32 s18, s10, 2
	s_cmp_lt_u32 s18, s9
	s_cbranch_scc0 .Lg_s2skip1
	s_cmp_gt_u32 s10, s9
	s_cbranch_scc1 .Lg_s2final1
	s_waitcnt vmcnt(21)
	v_cvt_pk_f16_f32 v250, v178, v179
	v_cvt_pk_f16_f32 v251, v180, v181
	ds_write_b64 v241, v[250:251] offset:19968
	buffer_load_dwordx4 v[178:181], v238, s[20:23], s42 offen nt
	s_waitcnt vmcnt(21)
	v_cvt_pk_f16_f32 v252, v182, v183
	v_cvt_pk_f16_f32 v253, v184, v185
	ds_write_b64 v241, v[252:253] offset:20568
	buffer_load_dwordx4 v[182:185], v238, s[24:27], s42 offen nt
	s_waitcnt vmcnt(21)
	v_cvt_pk_f16_f32 v250, v186, v187
	v_cvt_pk_f16_f32 v251, v188, v189
	ds_write_b64 v241, v[250:251] offset:21216
	buffer_load_dwordx4 v[186:189], v238, s[20:23], s14 offen nt
	s_waitcnt vmcnt(21)
	v_cvt_pk_f16_f32 v252, v190, v191
	v_cvt_pk_f16_f32 v253, v192, v193
	ds_write_b64 v241, v[252:253] offset:21816
	buffer_load_dwordx4 v[190:193], v238, s[24:27], s14 offen nt
	s_waitcnt vmcnt(21)
	v_cvt_pk_f16_f32 v250, v194, v195
	v_cvt_pk_f16_f32 v251, v196, v197
	ds_write_b64 v241, v[250:251] offset:22464
	buffer_load_dwordx4 v[194:197], v238, s[20:23], s15 offen nt
	s_waitcnt vmcnt(21)
	v_cvt_pk_f16_f32 v252, v198, v199
	v_cvt_pk_f16_f32 v253, v200, v201
	ds_write_b64 v241, v[252:253] offset:23064
	buffer_load_dwordx4 v[198:201], v238, s[24:27], s15 offen nt
	s_waitcnt vmcnt(21)
	v_cvt_pk_f16_f32 v250, v202, v203
	v_cvt_pk_f16_f32 v251, v204, v205
	ds_write_b64 v241, v[250:251] offset:23712
	buffer_load_dwordx4 v[202:205], v238, s[20:23], s16 offen nt
	s_waitcnt vmcnt(21)
	v_cvt_pk_f16_f32 v252, v206, v207
	v_cvt_pk_f16_f32 v253, v208, v209
	ds_write_b64 v241, v[252:253] offset:24312
	buffer_load_dwordx4 v[206:209], v238, s[24:27], s16 offen nt
	s_mov_b64 exec, s[34:35]
	s_waitcnt vmcnt(21)
	v_cvt_pk_f16_f32 v250, v210, v211
	v_cvt_pk_f16_f32 v251, v212, v213
	ds_write_b64 v242, v[250:251] offset:19968
	s_mov_b64 exec, -1
	buffer_load_dwordx4 v[210:213], v254, s[20:23], s12 offen nt
	s_mov_b64 exec, s[34:35]
	s_waitcnt vmcnt(21)
	v_cvt_pk_f16_f32 v252, v214, v215
	v_cvt_pk_f16_f32 v253, v216, v217
	ds_write_b64 v242, v[252:253] offset:20568
	s_mov_b64 exec, -1
	buffer_load_dwordx4 v[214:217], v254, s[24:27], s12 offen nt
	s_branch .Lg_s1done1
.Lg_s2final1:
	s_waitcnt vmcnt(21)
	v_cvt_pk_f16_f32 v250, v178, v179
	v_cvt_pk_f16_f32 v251, v180, v181
	ds_write_b64 v241, v[250:251] offset:19968
	s_waitcnt vmcnt(20)
	v_cvt_pk_f16_f32 v252, v182, v183
	v_cvt_pk_f16_f32 v253, v184, v185
	ds_write_b64 v241, v[252:253] offset:20568
	s_waitcnt vmcnt(19)
	v_cvt_pk_f16_f32 v250, v186, v187
	v_cvt_pk_f16_f32 v251, v188, v189
	ds_write_b64 v241, v[250:251] offset:21216
	s_waitcnt vmcnt(18)
	v_cvt_pk_f16_f32 v252, v190, v191
	v_cvt_pk_f16_f32 v253, v192, v193
	ds_write_b64 v241, v[252:253] offset:21816
	s_waitcnt vmcnt(17)
	v_cvt_pk_f16_f32 v250, v194, v195
	v_cvt_pk_f16_f32 v251, v196, v197
	ds_write_b64 v241, v[250:251] offset:22464
	s_waitcnt vmcnt(16)
	v_cvt_pk_f16_f32 v252, v198, v199
	v_cvt_pk_f16_f32 v253, v200, v201
	ds_write_b64 v241, v[252:253] offset:23064
	s_waitcnt vmcnt(15)
	v_cvt_pk_f16_f32 v250, v202, v203
	v_cvt_pk_f16_f32 v251, v204, v205
	ds_write_b64 v241, v[250:251] offset:23712
	s_waitcnt vmcnt(14)
	v_cvt_pk_f16_f32 v252, v206, v207
	v_cvt_pk_f16_f32 v253, v208, v209
	ds_write_b64 v241, v[252:253] offset:24312
	s_mov_b64 exec, s[34:35]
	s_waitcnt vmcnt(13)
	v_cvt_pk_f16_f32 v250, v210, v211
	v_cvt_pk_f16_f32 v251, v212, v213
	ds_write_b64 v242, v[250:251] offset:19968
	s_mov_b64 exec, -1
	s_mov_b64 exec, s[34:35]
	s_waitcnt vmcnt(12)
	v_cvt_pk_f16_f32 v252, v214, v215
	v_cvt_pk_f16_f32 v253, v216, v217
	ds_write_b64 v242, v[252:253] offset:20568
	s_mov_b64 exec, -1
	s_branch .Lg_s1done1
.Lg_s2skip1:
	s_cmp_gt_u32 s10, s9
	s_cbranch_scc1 .Lg_s1done1
	buffer_load_dwordx4 v[178:181], v238, s[20:23], s42 offen nt
	buffer_load_dwordx4 v[182:185], v238, s[24:27], s42 offen nt
	buffer_load_dwordx4 v[186:189], v238, s[20:23], s14 offen nt
	buffer_load_dwordx4 v[190:193], v238, s[24:27], s14 offen nt
	buffer_load_dwordx4 v[194:197], v238, s[20:23], s15 offen nt
	buffer_load_dwordx4 v[198:201], v238, s[24:27], s15 offen nt
	buffer_load_dwordx4 v[202:205], v238, s[20:23], s16 offen nt
	buffer_load_dwordx4 v[206:209], v238, s[24:27], s16 offen nt
	buffer_load_dwordx4 v[210:213], v254, s[20:23], s12 offen nt
	buffer_load_dwordx4 v[214:217], v254, s[24:27], s12 offen nt
